# RWKV scan serial chain: ring-slot test uses the done word read one step earlier (ds_read in the deferred publish block), slow spin path unchanged
# speedup vs baseline: 1.0112x; 1.0112x over previous
.LBB0_1302:
	s_sub_i32 s2, 0x7d, s18
	s_add_i32 s23, s18, 2
	s_and_b64 s[8:9], s[6:7], exec
	s_cselect_b32 s2, s23, s2
	s_add_i32 s8, s2, s19
	s_ashr_i32 s9, s8, 31
	s_lshl_b64 s[10:11], s[8:9], 13
	s_add_u32 s24, s20, s10
	s_addc_u32 s25, s21, s11
	v_lshlrev_b32_e32 v174, 1, v176
	v_lshl_add_u64 v[98:99], s[24:25], 0, v[174:175]
	s_lshl_b64 s[8:9], s[8:9], 8
	v_add_co_u32_e32 v102, vcc, s22, v98
	v_lshl_add_u64 v[110:111], v[178:179], 0, s[8:9]
	v_lshl_add_u64 v[112:113], v[180:181], 0, s[10:11]
	v_addc_co_u32_e32 v103, vcc, 0, v99, vcc
	global_load_dwordx4 v[142:145], v174, s[24:25]
	global_load_dwordx4 v[138:141], v174, s[24:25] offset:1024
	global_load_dwordx4 v[122:125], v174, s[24:25] offset:2048
	global_load_dwordx4 v[126:129], v174, s[24:25] offset:3072
	global_load_dwordx4 v[146:149], v[110:111], off
	global_load_dwordx4 v[134:137], v[110:111], off offset:64
	global_load_dwordx4 v[114:117], v206, s[24:25]
	global_load_dwordx4 v[118:121], v[102:103], off offset:1024
	global_load_dwordx4 v[98:101], v207, s[24:25]
	s_nop 0
	global_load_dwordx4 v[102:105], v[102:103], off offset:3072
	s_nop 0
	global_load_dwordx2 v[200:201], v[112:113], off
	global_load_dwordx2 v[198:199], v[112:113], off offset:512
	global_load_dwordx2 v[172:173], v[112:113], off offset:1024
	global_load_dwordx2 v[170:171], v[112:113], off offset:1536
	global_load_dwordx4 v[130:133], v[110:111], off offset:128
	s_nop 0
	global_load_dwordx4 v[110:113], v[110:111], off offset:192
	s_cmp_gt_u32 s18, 7
	s_cselect_b64 s[8:9], -1, 0
	s_cmp_lt_u32 s18, 8
	s_cbranch_scc1 .LBB0_1305
	s_add_i32 s10, s12, 0
	s_add_i32 s10, s10, 0x10020
	s_waitcnt lgkmcnt(0)
	v_add_u32_e32 v162, 8, v230
	v_cmp_lt_u32_e32 vcc, s18, v162
	s_cbranch_vccnz .LBB0_1305

.LBB0_1305:
	s_lshl_b32 s2, s18, 11
	s_and_b32 s2, s2, 0x3000
	v_add_u32_e32 v202, s2, v177
	v_cvt_pk_bf16_f32 v162, v158, v159
	v_cvt_pk_bf16_f32 v163, v160, v161
	v_cvt_pk_bf16_f32 v164, v154, v155
	v_cvt_pk_bf16_f32 v165, v156, v157
	v_cvt_pk_bf16_f32 v166, v150, v151
	v_cvt_pk_bf16_f32 v167, v152, v153
	v_cvt_pk_bf16_f32 v168, v106, v107
	v_cvt_pk_bf16_f32 v169, v108, v109
	ds_write2st64_b64 v202, v[162:163], v[164:165] offset1:1
	ds_write2st64_b64 v202, v[166:167], v[168:169] offset0:2 offset1:3
	s_nop 1
	s_or_b32 s24, s18, 1
	v_mov_b32_e32 v222, s12
	v_add_u32_e32 v222, 0x10000, v222
	v_add_u32_e32 v231, 32, v222
	v_mov_b32_e32 v223, s24
	s_waitcnt vmcnt(45)
	v_lshlrev_b32_e32 v202, 16, v188
	v_and_b32_e32 v203, 0xffff0000, v188
	s_waitcnt vmcnt(44)
	v_pk_fma_f32 v[46:47], v[158:159], v[46:47], v[202:203]
	v_lshlrev_b32_e32 v158, 16, v189
	v_and_b32_e32 v159, 0xffff0000, v189
	v_pk_fma_f32 v[48:49], v[160:161], v[48:49], v[158:159]
	s_sub_i32 s2, 0x7c, s18
	s_add_i32 s10, s18, 3
	v_mfma_f32_16x16x32_bf16 v[38:41], v[38:41], v[162:165], v[46:49]
	s_and_b64 s[26:27], s[6:7], exec
	s_cselect_b32 s2, s10, s2
	s_add_i32 s26, s2, s19
	v_mfma_f32_16x16x32_bf16 v[158:161], v[30:33], v[166:169], v[38:41]
	s_waitcnt lgkmcnt(0)
	s_mov_b64 s[98:99], exec
	s_mov_b64 exec, s[0:1]
	ds_write_b32 v222, v223
	s_mov_b64 exec, s[98:99]
	ds_read_b32 v230, v231
	s_waitcnt vmcnt(41)
	v_lshlrev_b32_e32 v30, 16, v186
	v_and_b32_e32 v31, 0xffff0000, v186
	v_lshlrev_b32_e32 v32, 16, v187
	v_and_b32_e32 v33, 0xffff0000, v187
	s_waitcnt vmcnt(40)
	v_pk_fma_f32 v[30:31], v[154:155], v[42:43], v[30:31]
	v_pk_fma_f32 v[32:33], v[156:157], v[44:45], v[32:33]
	s_ashr_i32 s27, s26, 31
	s_lshl_b64 s[28:29], s[26:27], 13
	v_mfma_f32_16x16x32_bf16 v[18:21], v[18:21], v[162:165], v[30:33]
	s_add_u32 s30, s20, s28
	s_addc_u32 s31, s21, s29
	s_lshl_b64 s[26:27], s[26:27], 8
	v_mfma_f32_16x16x32_bf16 v[154:157], v[22:25], v[166:169], v[18:21]
	v_lshl_add_u64 v[30:31], v[178:179], 0, s[26:27]
	v_lshl_add_u64 v[32:33], v[180:181], 0, s[28:29]
	s_waitcnt vmcnt(37)
	s_nop 0
	v_lshlrev_b32_e32 v18, 16, v182
	v_and_b32_e32 v19, 0xffff0000, v182
	v_lshlrev_b32_e32 v20, 16, v183
	v_and_b32_e32 v21, 0xffff0000, v183
	s_waitcnt vmcnt(36)
	v_pk_fma_f32 v[18:19], v[150:151], v[26:27], v[18:19]
	v_pk_fma_f32 v[20:21], v[152:153], v[28:29], v[20:21]
	s_nop 1
	v_mfma_f32_16x16x32_bf16 v[2:5], v[2:5], v[162:165], v[18:21]
	v_mfma_f32_16x16x32_bf16 v[150:153], v[14:17], v[166:169], v[2:5]
	s_waitcnt vmcnt(33)
	s_nop 5
	v_lshlrev_b32_e32 v2, 16, v184
	v_and_b32_e32 v3, 0xffff0000, v184
	v_lshlrev_b32_e32 v4, 16, v185
	v_and_b32_e32 v5, 0xffff0000, v185
	s_waitcnt vmcnt(32)
	v_pk_fma_f32 v[2:3], v[106:107], v[34:35], v[2:3]
	v_pk_fma_f32 v[4:5], v[108:109], v[36:37], v[4:5]
	global_load_dwordx4 v[42:45], v174, s[30:31]
	global_load_dwordx4 v[34:37], v174, s[30:31] offset:1024
	v_mfma_f32_16x16x32_bf16 v[2:5], v[6:9], v[162:165], v[2:5]
	v_lshl_add_u64 v[6:7], s[30:31], 0, v[174:175]
	v_mfma_f32_16x16x32_bf16 v[106:109], v[10:13], v[166:169], v[2:5]
	v_add_co_u32_e32 v10, vcc, 0x1000, v6
	global_load_dwordx2 v[188:189], v[32:33], off
	global_load_dwordx4 v[46:49], v[30:31], off
	global_load_dwordx4 v[18:21], v174, s[30:31] offset:2048
	global_load_dwordx4 v[22:25], v174, s[30:31] offset:3072
	global_load_dwordx2 v[186:187], v[32:33], off offset:512
	global_load_dwordx4 v[38:41], v[30:31], off offset:64
	global_load_dwordx4 v[2:5], v206, s[30:31]
	v_addc_co_u32_e32 v11, vcc, 0, v7, vcc
	global_load_dwordx4 v[14:17], v[10:11], off offset:1024
	global_load_dwordx2 v[182:183], v[32:33], off offset:1024
	global_load_dwordx4 v[26:29], v[30:31], off offset:128
	global_load_dwordx4 v[6:9], v207, s[30:31]
	s_nop 0
	global_load_dwordx4 v[10:13], v[10:11], off offset:3072
	s_nop 0
	global_load_dwordx2 v[184:185], v[32:33], off offset:1536
	s_nop 0
	global_load_dwordx4 v[30:33], v[30:31], off offset:192
	s_andn2_b64 vcc, exec, s[8:9]
	s_cbranch_vccnz .LBB0_1310
	s_add_i32 s8, s12, 0
	s_add_i32 s8, s8, 0x10020
	s_waitcnt lgkmcnt(0)
	v_add_u32_e32 v162, 8, v230
	v_cmp_lt_u32_e32 vcc, s24, v162
	s_cbranch_vccnz .LBB0_1310

.LBB0_1310:
	s_lshl_b32 s2, s24, 11
	s_and_b32 s2, s2, 0x3800
	v_add_u32_e32 v202, s2, v177
	v_cvt_pk_bf16_f32 v162, v158, v159
	v_cvt_pk_bf16_f32 v163, v160, v161
	v_cvt_pk_bf16_f32 v164, v154, v155
	v_cvt_pk_bf16_f32 v165, v156, v157
	v_cvt_pk_bf16_f32 v166, v150, v151
	v_cvt_pk_bf16_f32 v167, v152, v153
	v_cvt_pk_bf16_f32 v168, v106, v107
	v_cvt_pk_bf16_f32 v169, v108, v109
	ds_write2st64_b64 v202, v[162:163], v[164:165] offset1:1
	ds_write2st64_b64 v202, v[166:167], v[168:169] offset0:2 offset1:3
	s_nop 1
	v_mov_b32_e32 v222, s12
	v_add_u32_e32 v222, 0x10000, v222
	v_add_u32_e32 v231, 32, v222
	v_mov_b32_e32 v223, s23
	s_waitcnt vmcnt(37)
	v_lshlrev_b32_e32 v202, 16, v196
	v_and_b32_e32 v203, 0xffff0000, v196
	s_waitcnt vmcnt(44)
	v_pk_fma_f32 v[94:95], v[94:95], v[158:159], v[202:203]
	v_lshlrev_b32_e32 v158, 16, v197
	v_and_b32_e32 v159, 0xffff0000, v197
	v_pk_fma_f32 v[96:97], v[96:97], v[160:161], v[158:159]
	s_sub_i32 s2, 0x7b, s18
	s_add_i32 s11, s18, 4
	v_mfma_f32_16x16x32_bf16 v[78:81], v[78:81], v[162:165], v[94:97]
	s_and_b64 s[8:9], s[6:7], exec
	s_cselect_b32 s2, s11, s2
	s_add_i32 s8, s2, s19
	v_mfma_f32_16x16x32_bf16 v[158:161], v[70:73], v[166:169], v[78:81]
	s_waitcnt lgkmcnt(0)
	s_mov_b64 s[98:99], exec
	s_mov_b64 exec, s[0:1]
	ds_write_b32 v222, v223
	s_mov_b64 exec, s[98:99]
	ds_read_b32 v230, v231
	s_waitcnt vmcnt(36)
	v_lshlrev_b32_e32 v70, 16, v194
	v_and_b32_e32 v71, 0xffff0000, v194
	v_lshlrev_b32_e32 v72, 16, v195
	v_and_b32_e32 v73, 0xffff0000, v195
	s_waitcnt vmcnt(40)
	v_pk_fma_f32 v[70:71], v[82:83], v[154:155], v[70:71]
	v_pk_fma_f32 v[72:73], v[84:85], v[156:157], v[72:73]
	s_ashr_i32 s9, s8, 31
	s_lshl_b64 s[24:25], s[8:9], 13
	v_mfma_f32_16x16x32_bf16 v[50:53], v[50:53], v[162:165], v[70:73]
	s_add_u32 s26, s20, s24
	s_addc_u32 s27, s21, s25
	s_lshl_b64 s[8:9], s[8:9], 8
	v_mfma_f32_16x16x32_bf16 v[94:97], v[58:61], v[166:169], v[50:53]
	s_cmp_lt_u32 s18, 6
	s_waitcnt vmcnt(35)
	s_nop 1
	v_lshlrev_b32_e32 v50, 16, v190
	v_and_b32_e32 v51, 0xffff0000, v190
	v_lshlrev_b32_e32 v52, 16, v191
	v_and_b32_e32 v53, 0xffff0000, v191
	s_waitcnt vmcnt(33)
	v_pk_fma_f32 v[50:51], v[86:87], v[150:151], v[50:51]
	v_pk_fma_f32 v[52:53], v[88:89], v[152:153], v[52:53]
	global_load_dwordx4 v[86:89], v174, s[26:27]
	global_load_dwordx4 v[78:81], v174, s[26:27] offset:1024
	v_mfma_f32_16x16x32_bf16 v[50:53], v[54:57], v[162:165], v[50:53]
	v_lshl_add_u64 v[54:55], s[26:27], 0, v[174:175]
	v_mfma_f32_16x16x32_bf16 v[150:153], v[74:77], v[166:169], v[50:53]
	v_lshl_add_u64 v[74:75], v[178:179], 0, s[8:9]
	v_lshl_add_u64 v[76:77], v[180:181], 0, s[24:25]
	s_waitcnt vmcnt(35)
	s_nop 2
	v_lshlrev_b32_e32 v50, 16, v192
	v_and_b32_e32 v51, 0xffff0000, v192
	v_lshlrev_b32_e32 v52, 16, v193
	v_and_b32_e32 v53, 0xffff0000, v193
	s_waitcnt vmcnt(34)
	v_pk_fma_f32 v[50:51], v[90:91], v[106:107], v[50:51]
	v_pk_fma_f32 v[52:53], v[92:93], v[108:109], v[52:53]
	v_add_co_u32_e32 v106, vcc, 0x1000, v54
	s_nop 0
	v_mfma_f32_16x16x32_bf16 v[50:53], v[62:65], v[162:165], v[50:53]
	v_addc_co_u32_e32 v107, vcc, 0, v55, vcc
	v_mfma_f32_16x16x32_bf16 v[154:157], v[66:69], v[166:169], v[50:53]
	global_load_dwordx2 v[196:197], v[76:77], off
	global_load_dwordx4 v[90:93], v[74:75], off
	global_load_dwordx4 v[62:65], v174, s[26:27] offset:2048
	global_load_dwordx4 v[66:69], v174, s[26:27] offset:3072
	global_load_dwordx2 v[194:195], v[76:77], off offset:512
	global_load_dwordx4 v[82:85], v[74:75], off offset:64
	global_load_dwordx4 v[50:53], v206, s[26:27]
	global_load_dwordx4 v[58:61], v[106:107], off offset:1024
	global_load_dwordx2 v[190:191], v[76:77], off offset:1024
	global_load_dwordx4 v[70:73], v[74:75], off offset:128
	global_load_dwordx4 v[54:57], v207, s[26:27]
	s_nop 0
	global_load_dwordx4 v[106:109], v[106:107], off offset:3072
	s_nop 0
	global_load_dwordx2 v[192:193], v[76:77], off offset:1536
	s_nop 0
	global_load_dwordx4 v[74:77], v[74:75], off offset:192
	s_cbranch_scc1 .LBB0_1315
	s_add_i32 s8, s12, 0
	s_add_i32 s8, s8, 0x10020
	s_waitcnt lgkmcnt(0)
	v_add_u32_e32 v162, 8, v230
	v_cmp_lt_u32_e32 vcc, s23, v162
	s_cbranch_vccnz .LBB0_1315

.LBB0_1315:
	s_lshl_b32 s2, s23, 11
	s_and_b32 s2, s2, 0x3000
	v_add_u32_e32 v202, s2, v177
	v_cvt_pk_bf16_f32 v162, v158, v159
	v_cvt_pk_bf16_f32 v163, v160, v161
	v_cvt_pk_bf16_f32 v164, v94, v95
	v_cvt_pk_bf16_f32 v165, v96, v97
	v_cvt_pk_bf16_f32 v166, v150, v151
	v_cvt_pk_bf16_f32 v167, v152, v153
	v_cvt_pk_bf16_f32 v168, v154, v155
	v_cvt_pk_bf16_f32 v169, v156, v157
	ds_write2st64_b64 v202, v[162:163], v[164:165] offset1:1
	ds_write2st64_b64 v202, v[166:167], v[168:169] offset0:2 offset1:3
	s_nop 1
	v_mov_b32_e32 v222, s12
	v_add_u32_e32 v222, 0x10000, v222
	v_add_u32_e32 v231, 32, v222
	v_mov_b32_e32 v223, s10
	s_waitcnt vmcnt(37)
	v_lshlrev_b32_e32 v202, 16, v200
	v_and_b32_e32 v203, 0xffff0000, v200
	v_pk_fma_f32 v[146:147], v[146:147], v[158:159], v[202:203]
	v_lshlrev_b32_e32 v158, 16, v201
	v_and_b32_e32 v159, 0xffff0000, v201
	v_pk_fma_f32 v[148:149], v[148:149], v[160:161], v[158:159]
	s_sub_i32 s2, 0x7a, s18
	s_add_i32 s23, s18, 5
	v_mfma_f32_16x16x32_bf16 v[142:145], v[142:145], v[162:165], v[146:149]
	s_and_b64 s[8:9], s[6:7], exec
	s_cselect_b32 s2, s23, s2
	s_add_i32 s8, s2, s19
	v_mfma_f32_16x16x32_bf16 v[158:161], v[138:141], v[166:169], v[142:145]
	s_waitcnt lgkmcnt(0)
	s_mov_b64 s[98:99], exec
	s_mov_b64 exec, s[0:1]
	ds_write_b32 v222, v223
	s_mov_b64 exec, s[98:99]
	ds_read_b32 v230, v231
	s_waitcnt vmcnt(36)
	v_lshlrev_b32_e32 v138, 16, v198
	v_and_b32_e32 v139, 0xffff0000, v198
	v_pk_fma_f32 v[94:95], v[134:135], v[94:95], v[138:139]
	v_lshlrev_b32_e32 v134, 16, v199
	v_and_b32_e32 v135, 0xffff0000, v199
	v_pk_fma_f32 v[96:97], v[136:137], v[96:97], v[134:135]
	s_ashr_i32 s9, s8, 31
	s_lshl_b64 s[24:25], s[8:9], 13
	v_mfma_f32_16x16x32_bf16 v[94:97], v[122:125], v[162:165], v[94:97]
	s_waitcnt vmcnt(35)
	v_lshlrev_b32_e32 v122, 16, v172
	v_and_b32_e32 v123, 0xffff0000, v172
	v_lshlrev_b32_e32 v124, 16, v173
	v_and_b32_e32 v125, 0xffff0000, v173
	s_waitcnt vmcnt(33)
	v_pk_fma_f32 v[122:123], v[130:131], v[150:151], v[122:123]
	v_pk_fma_f32 v[124:125], v[132:133], v[152:153], v[124:125]
	s_add_u32 s26, s20, s24
	s_addc_u32 s27, s21, s25
	v_mfma_f32_16x16x32_bf16 v[114:117], v[114:117], v[162:165], v[122:125]
	s_lshl_b64 s[8:9], s[8:9], 8
	v_lshl_add_u64 v[130:131], v[178:179], 0, s[8:9]
	v_lshl_add_u64 v[132:133], v[180:181], 0, s[24:25]
	v_mfma_f32_16x16x32_bf16 v[150:153], v[118:121], v[166:169], v[114:117]
	global_load_dwordx4 v[142:145], v174, s[26:27]
	global_load_dwordx4 v[134:137], v174, s[26:27] offset:1024
	s_cmp_lt_u32 s18, 5
	s_nop 0
	v_lshlrev_b32_e32 v114, 16, v170
	v_and_b32_e32 v115, 0xffff0000, v170
	s_waitcnt vmcnt(34)
	v_pk_fma_f32 v[110:111], v[110:111], v[154:155], v[114:115]
	v_lshlrev_b32_e32 v114, 16, v171
	v_and_b32_e32 v115, 0xffff0000, v171
	v_pk_fma_f32 v[112:113], v[112:113], v[156:157], v[114:115]
	v_mfma_f32_16x16x32_bf16 v[94:97], v[126:129], v[166:169], v[94:97]
	s_nop 0
	v_mfma_f32_16x16x32_bf16 v[98:101], v[98:101], v[162:165], v[110:113]
	v_mfma_f32_16x16x32_bf16 v[154:157], v[102:105], v[166:169], v[98:101]
	global_load_dwordx2 v[204:205], v[132:133], off
	global_load_dwordx4 v[146:149], v[130:131], off
	global_load_dwordx4 v[118:121], v174, s[26:27] offset:2048
	global_load_dwordx4 v[122:125], v174, s[26:27] offset:3072
	global_load_dwordx2 v[202:203], v[132:133], off offset:512
	global_load_dwordx4 v[138:141], v[130:131], off offset:64
	global_load_dwordx4 v[102:105], v206, s[26:27]
	v_lshl_add_u64 v[98:99], s[26:27], 0, v[174:175]
	v_add_co_u32_e32 v98, vcc, 0x1000, v98
	s_nop 1
	v_addc_co_u32_e32 v99, vcc, 0, v99, vcc
	global_load_dwordx4 v[114:117], v[98:99], off offset:1024
	global_load_dwordx2 v[198:199], v[132:133], off offset:1024
	global_load_dwordx4 v[126:129], v[130:131], off offset:128
	global_load_dwordx4 v[110:113], v207, s[26:27]
	s_nop 0
	global_load_dwordx4 v[98:101], v[98:99], off offset:3072
	s_nop 0
	global_load_dwordx2 v[200:201], v[132:133], off offset:1536
	s_nop 0
	global_load_dwordx4 v[130:133], v[130:131], off offset:192
	s_cbranch_scc1 .LBB0_1320
	s_add_i32 s8, s12, 0
	s_add_i32 s8, s8, 0x10020
	s_waitcnt lgkmcnt(0)
	v_add_u32_e32 v162, 8, v230
	v_cmp_lt_u32_e32 vcc, s10, v162
	s_cbranch_vccnz .LBB0_1320

.LBB0_1320:
	s_lshl_b32 s2, s10, 11
	s_and_b32 s2, s2, 0x3800
	v_add_u32_e32 v170, s2, v177
	v_cvt_pk_bf16_f32 v162, v158, v159
	v_cvt_pk_bf16_f32 v163, v160, v161
	v_cvt_pk_bf16_f32 v164, v94, v95
	v_cvt_pk_bf16_f32 v165, v96, v97
	v_cvt_pk_bf16_f32 v166, v150, v151
	v_cvt_pk_bf16_f32 v167, v152, v153
	v_cvt_pk_bf16_f32 v168, v154, v155
	v_cvt_pk_bf16_f32 v169, v156, v157
	ds_write2st64_b64 v170, v[162:163], v[164:165] offset1:1
	ds_write2st64_b64 v170, v[166:167], v[168:169] offset0:2 offset1:3
	s_nop 1
	v_mov_b32_e32 v222, s12
	v_add_u32_e32 v222, 0x10000, v222
	v_add_u32_e32 v231, 32, v222
	v_mov_b32_e32 v223, s11
	s_waitcnt vmcnt(45)
	v_lshlrev_b32_e32 v170, 16, v188
	v_and_b32_e32 v171, 0xffff0000, v188
	s_waitcnt vmcnt(44)
	v_pk_fma_f32 v[46:47], v[46:47], v[158:159], v[170:171]
	v_lshlrev_b32_e32 v158, 16, v189
	v_and_b32_e32 v159, 0xffff0000, v189
	v_pk_fma_f32 v[48:49], v[48:49], v[160:161], v[158:159]
	s_sub_i32 s2, 0x79, s18
	s_add_i32 s10, s18, 6
	v_mfma_f32_16x16x32_bf16 v[42:45], v[42:45], v[162:165], v[46:49]
	s_and_b64 s[8:9], s[6:7], exec
	s_cselect_b32 s2, s10, s2
	s_add_i32 s8, s2, s19
	v_mfma_f32_16x16x32_bf16 v[158:161], v[34:37], v[166:169], v[42:45]
	s_waitcnt lgkmcnt(0)
	s_mov_b64 s[98:99], exec
	s_mov_b64 exec, s[0:1]
	ds_write_b32 v222, v223
	s_mov_b64 exec, s[98:99]
	ds_read_b32 v230, v231
	s_waitcnt vmcnt(41)
	v_lshlrev_b32_e32 v34, 16, v186
	v_and_b32_e32 v35, 0xffff0000, v186
	v_lshlrev_b32_e32 v36, 16, v187
	v_and_b32_e32 v37, 0xffff0000, v187
	s_waitcnt vmcnt(40)
	v_pk_fma_f32 v[34:35], v[38:39], v[94:95], v[34:35]
	v_pk_fma_f32 v[36:37], v[40:41], v[96:97], v[36:37]
	s_ashr_i32 s9, s8, 31
	s_lshl_b64 s[24:25], s[8:9], 13
	v_mfma_f32_16x16x32_bf16 v[18:21], v[18:21], v[162:165], v[34:37]
	s_add_u32 s26, s20, s24
	s_addc_u32 s27, s21, s25
	s_lshl_b64 s[8:9], s[8:9], 8
	v_mfma_f32_16x16x32_bf16 v[94:97], v[22:25], v[166:169], v[18:21]
	v_lshl_add_u64 v[34:35], v[178:179], 0, s[8:9]
	v_lshl_add_u64 v[36:37], v[180:181], 0, s[24:25]
	s_cmp_lt_u32 s18, 4
	s_waitcnt vmcnt(37)
	v_lshlrev_b32_e32 v18, 16, v182
	v_and_b32_e32 v19, 0xffff0000, v182
	v_lshlrev_b32_e32 v20, 16, v183
	v_and_b32_e32 v21, 0xffff0000, v183
	s_waitcnt vmcnt(36)
	v_pk_fma_f32 v[18:19], v[26:27], v[150:151], v[18:19]
	v_pk_fma_f32 v[20:21], v[28:29], v[152:153], v[20:21]
	s_nop 1
	v_mfma_f32_16x16x32_bf16 v[2:5], v[2:5], v[162:165], v[18:21]
	v_mfma_f32_16x16x32_bf16 v[150:153], v[14:17], v[166:169], v[2:5]
	s_waitcnt vmcnt(33)
	s_nop 5
	v_lshlrev_b32_e32 v2, 16, v184
	v_and_b32_e32 v3, 0xffff0000, v184
	v_lshlrev_b32_e32 v4, 16, v185
	v_and_b32_e32 v5, 0xffff0000, v185
	s_waitcnt vmcnt(32)
	v_pk_fma_f32 v[2:3], v[30:31], v[154:155], v[2:3]
	v_pk_fma_f32 v[4:5], v[32:33], v[156:157], v[4:5]
	global_load_dwordx4 v[38:41], v174, s[26:27]
	global_load_dwordx4 v[30:33], v174, s[26:27] offset:1024
	v_mfma_f32_16x16x32_bf16 v[2:5], v[6:9], v[162:165], v[2:5]
	v_lshl_add_u64 v[6:7], s[26:27], 0, v[174:175]
	v_mfma_f32_16x16x32_bf16 v[154:157], v[10:13], v[166:169], v[2:5]
	v_add_co_u32_e32 v10, vcc, 0x1000, v6
	global_load_dwordx2 v[188:189], v[36:37], off
	global_load_dwordx4 v[46:49], v[34:35], off
	global_load_dwordx4 v[18:21], v174, s[26:27] offset:2048
	global_load_dwordx4 v[22:25], v174, s[26:27] offset:3072
	global_load_dwordx2 v[186:187], v[36:37], off offset:512
	global_load_dwordx4 v[42:45], v[34:35], off offset:64
	global_load_dwordx4 v[2:5], v206, s[26:27]
	v_addc_co_u32_e32 v11, vcc, 0, v7, vcc
	global_load_dwordx4 v[14:17], v[10:11], off offset:1024
	global_load_dwordx2 v[182:183], v[36:37], off offset:1024
	global_load_dwordx4 v[26:29], v[34:35], off offset:128
	global_load_dwordx4 v[6:9], v207, s[26:27]
	s_nop 0
	global_load_dwordx4 v[10:13], v[10:11], off offset:3072
	s_nop 0
	global_load_dwordx2 v[184:185], v[36:37], off offset:1536
	s_nop 0
	global_load_dwordx4 v[34:37], v[34:35], off offset:192
	s_cbranch_scc1 .LBB0_1325
	s_add_i32 s8, s12, 0
	s_add_i32 s8, s8, 0x10020
	s_waitcnt lgkmcnt(0)
	v_add_u32_e32 v162, 8, v230
	v_cmp_lt_u32_e32 vcc, s11, v162
	s_cbranch_vccnz .LBB0_1325

.LBB0_1325:
	s_lshl_b32 s2, s11, 11
	s_and_b32 s2, s2, 0x3000
	v_add_u32_e32 v162, s2, v177
	v_cvt_pk_bf16_f32 v170, v158, v159
	v_cvt_pk_bf16_f32 v171, v160, v161
	v_cvt_pk_bf16_f32 v172, v94, v95
	v_cvt_pk_bf16_f32 v173, v96, v97
	v_cvt_pk_bf16_f32 v166, v150, v151
	v_cvt_pk_bf16_f32 v167, v152, v153
	v_cvt_pk_bf16_f32 v168, v154, v155
	v_cvt_pk_bf16_f32 v169, v156, v157
	ds_write2st64_b64 v162, v[170:171], v[172:173] offset1:1
	ds_write2st64_b64 v162, v[166:167], v[168:169] offset0:2 offset1:3
	s_nop 1
	v_mov_b32_e32 v222, s12
	v_add_u32_e32 v222, 0x10000, v222
	v_add_u32_e32 v231, 32, v222
	v_mov_b32_e32 v223, s23
	s_waitcnt vmcnt(45)
	v_lshlrev_b32_e32 v162, 16, v196
	v_and_b32_e32 v163, 0xffff0000, v196
	s_waitcnt vmcnt(44)
	v_pk_fma_f32 v[90:91], v[90:91], v[158:159], v[162:163]
	v_lshlrev_b32_e32 v158, 16, v197
	v_and_b32_e32 v159, 0xffff0000, v197
	v_pk_fma_f32 v[92:93], v[92:93], v[160:161], v[158:159]
	s_sub_i32 s2, 0x78, s18
	s_add_i32 s3, s18, 7
	v_mfma_f32_16x16x32_bf16 v[86:89], v[86:89], v[170:173], v[90:93]
	s_and_b64 s[8:9], s[6:7], exec
	s_cselect_b32 s2, s3, s2
	s_add_i32 s8, s2, s19
	v_mfma_f32_16x16x32_bf16 v[158:161], v[78:81], v[166:169], v[86:89]
	s_waitcnt lgkmcnt(0)
	s_mov_b64 s[98:99], exec
	s_mov_b64 exec, s[0:1]
	ds_write_b32 v222, v223
	s_mov_b64 exec, s[98:99]
	ds_read_b32 v230, v231
	s_waitcnt vmcnt(41)
	v_lshlrev_b32_e32 v78, 16, v194
	v_and_b32_e32 v79, 0xffff0000, v194
	v_lshlrev_b32_e32 v80, 16, v195
	v_and_b32_e32 v81, 0xffff0000, v195
	s_waitcnt vmcnt(40)
	v_pk_fma_f32 v[78:79], v[82:83], v[94:95], v[78:79]
	v_pk_fma_f32 v[80:81], v[84:85], v[96:97], v[80:81]
	s_ashr_i32 s9, s8, 31
	s_lshl_b64 s[24:25], s[8:9], 13
	v_mfma_f32_16x16x32_bf16 v[62:65], v[62:65], v[170:173], v[78:81]
	s_add_u32 s26, s20, s24
	s_addc_u32 s27, s21, s25
	s_lshl_b64 s[8:9], s[8:9], 8
	v_mfma_f32_16x16x32_bf16 v[162:165], v[66:69], v[166:169], v[62:65]
	v_lshl_add_u64 v[90:91], v[178:179], 0, s[8:9]
	v_lshl_add_u64 v[86:87], v[180:181], 0, s[24:25]
	s_cmp_lt_u32 s18, 3
	s_waitcnt vmcnt(37)
	v_lshlrev_b32_e32 v62, 16, v190
	v_and_b32_e32 v63, 0xffff0000, v190
	v_lshlrev_b32_e32 v64, 16, v191
	v_and_b32_e32 v65, 0xffff0000, v191
	s_waitcnt vmcnt(36)
	v_pk_fma_f32 v[62:63], v[70:71], v[150:151], v[62:63]
	v_pk_fma_f32 v[64:65], v[72:73], v[152:153], v[64:65]
	global_load_dwordx4 v[78:81], v174, s[26:27]
	global_load_dwordx4 v[70:73], v174, s[26:27] offset:1024
	v_mfma_f32_16x16x32_bf16 v[50:53], v[50:53], v[170:173], v[62:65]
	v_mfma_f32_16x16x32_bf16 v[150:153], v[58:61], v[166:169], v[50:53]
	s_waitcnt vmcnt(35)
	s_nop 5
	v_lshlrev_b32_e32 v50, 16, v192
	v_and_b32_e32 v51, 0xffff0000, v192
	v_lshlrev_b32_e32 v52, 16, v193
	v_and_b32_e32 v53, 0xffff0000, v193
	s_waitcnt vmcnt(34)
	v_pk_fma_f32 v[50:51], v[74:75], v[154:155], v[50:51]
	v_pk_fma_f32 v[52:53], v[76:77], v[156:157], v[52:53]
	s_nop 1
	v_mfma_f32_16x16x32_bf16 v[154:157], v[54:57], v[170:173], v[50:53]
	v_lshl_add_u64 v[54:55], s[26:27], 0, v[174:175]
	v_add_co_u32_e32 v66, vcc, 0x1000, v54
	s_nop 0
	global_load_dwordx4 v[50:53], v174, s[26:27] offset:2048
	global_load_dwordx4 v[58:61], v174, s[26:27] offset:3072
	global_load_dwordx4 v[94:97], v[90:91], off
	global_load_dwordx4 v[82:85], v[90:91], off offset:64
	v_addc_co_u32_e32 v67, vcc, 0, v55, vcc
	global_load_dwordx4 v[54:57], v206, s[26:27]
	global_load_dwordx4 v[62:65], v207, s[26:27]
	global_load_dwordx4 v[74:77], v[66:67], off offset:1024
	s_nop 0
	global_load_dwordx4 v[66:69], v[66:67], off offset:3072
	s_nop 0
	global_load_dwordx2 v[196:197], v[86:87], off
	global_load_dwordx2 v[194:195], v[86:87], off offset:512
	global_load_dwordx2 v[190:191], v[86:87], off offset:1024
	global_load_dwordx2 v[192:193], v[86:87], off offset:1536
	s_nop 0
	global_load_dwordx4 v[86:89], v[90:91], off offset:128
	s_nop 0
	global_load_dwordx4 v[90:93], v[90:91], off offset:192
	v_mfma_f32_16x16x32_bf16 v[106:109], v[106:109], v[166:169], v[154:157]
	s_cbranch_scc1 .LBB0_1330
	s_add_i32 s8, s12, 0
	s_add_i32 s8, s8, 0x10020
	s_waitcnt lgkmcnt(0)
	v_add_u32_e32 v154, 8, v230
	v_cmp_lt_u32_e32 vcc, s23, v154
	s_cbranch_vccnz .LBB0_1330

.LBB0_1330:
	s_lshl_b32 s2, s23, 11
	s_and_b32 s2, s2, 0x3800
	v_add_u32_e32 v154, s2, v177
	v_cvt_pk_bf16_f32 v170, v158, v159
	v_cvt_pk_bf16_f32 v171, v160, v161
	v_cvt_pk_bf16_f32 v172, v162, v163
	v_cvt_pk_bf16_f32 v173, v164, v165
	v_cvt_pk_bf16_f32 v166, v150, v151
	v_cvt_pk_bf16_f32 v167, v152, v153
	v_cvt_pk_bf16_f32 v168, v106, v107
	v_cvt_pk_bf16_f32 v169, v108, v109
	ds_write2st64_b64 v154, v[170:171], v[172:173] offset1:1
	ds_write2st64_b64 v154, v[166:167], v[168:169] offset0:2 offset1:3
	s_nop 1
	v_mov_b32_e32 v222, s12
	v_add_u32_e32 v222, 0x10000, v222
	v_add_u32_e32 v231, 32, v222
	v_mov_b32_e32 v223, s10
	s_waitcnt vmcnt(45)
	v_lshlrev_b32_e32 v154, 16, v204
	v_and_b32_e32 v155, 0xffff0000, v204
	s_waitcnt vmcnt(44)
	v_pk_fma_f32 v[146:147], v[146:147], v[158:159], v[154:155]
	v_lshlrev_b32_e32 v154, 16, v205
	v_and_b32_e32 v155, 0xffff0000, v205
	v_pk_fma_f32 v[148:149], v[148:149], v[160:161], v[154:155]
	s_cmpk_lt_u32 s18, 0x78
	s_nop 0
	v_mfma_f32_16x16x32_bf16 v[142:145], v[142:145], v[170:173], v[146:149]
	v_mfma_f32_16x16x32_bf16 v[158:161], v[134:137], v[166:169], v[142:145]
	s_waitcnt lgkmcnt(0)
	s_mov_b64 s[98:99], exec
	s_mov_b64 exec, s[0:1]
	ds_write_b32 v222, v223
	s_mov_b64 exec, s[98:99]
	ds_read_b32 v230, v231
	s_waitcnt vmcnt(41)
	v_lshlrev_b32_e32 v134, 16, v202
	v_and_b32_e32 v135, 0xffff0000, v202
	v_lshlrev_b32_e32 v136, 16, v203
	v_and_b32_e32 v137, 0xffff0000, v203
	s_waitcnt vmcnt(40)
	v_pk_fma_f32 v[134:135], v[138:139], v[162:163], v[134:135]
	v_pk_fma_f32 v[136:137], v[140:141], v[164:165], v[136:137]
	s_nop 1
	v_mfma_f32_16x16x32_bf16 v[118:121], v[118:121], v[170:173], v[134:137]
	v_mfma_f32_16x16x32_bf16 v[154:157], v[122:125], v[166:169], v[118:121]
	s_waitcnt vmcnt(37)
	s_nop 5
	v_lshlrev_b32_e32 v118, 16, v198
	v_and_b32_e32 v119, 0xffff0000, v198
	v_lshlrev_b32_e32 v120, 16, v199
	v_and_b32_e32 v121, 0xffff0000, v199
	s_waitcnt vmcnt(36)
	v_pk_fma_f32 v[118:119], v[126:127], v[150:151], v[118:119]
	v_pk_fma_f32 v[120:121], v[128:129], v[152:153], v[120:121]
	s_nop 1
	v_mfma_f32_16x16x32_bf16 v[102:105], v[102:105], v[170:173], v[118:121]
	v_mfma_f32_16x16x32_bf16 v[150:153], v[114:117], v[166:169], v[102:105]
	s_waitcnt vmcnt(33)
	s_nop 5
	v_lshlrev_b32_e32 v102, 16, v200
	v_and_b32_e32 v103, 0xffff0000, v200
	v_lshlrev_b32_e32 v104, 16, v201
	v_and_b32_e32 v105, 0xffff0000, v201
	s_waitcnt vmcnt(32)
	v_pk_fma_f32 v[102:103], v[130:131], v[106:107], v[102:103]
	v_pk_fma_f32 v[104:105], v[132:133], v[108:109], v[104:105]
	s_nop 1
	v_mfma_f32_16x16x32_bf16 v[102:105], v[110:113], v[170:173], v[102:105]
	v_mfma_f32_16x16x32_bf16 v[106:109], v[98:101], v[166:169], v[102:105]
	s_cbranch_scc0 .LBB0_1334
	s_mov_b32 s18, s10
	s_branch .LBB0_1302

.LBB0_3620:
	s_sub_i32 s12, 0x7d, s20
	s_add_i32 s16, s20, 2
	s_and_b64 s[2:3], s[6:7], exec
	s_cselect_b32 s2, s16, s12
	s_add_i32 s2, s2, s21
	s_ashr_i32 s3, s2, 31
	s_lshl_b64 s[12:13], s[2:3], 13
	s_add_u32 s14, s22, s12
	s_addc_u32 s15, s23, s13
	v_lshlrev_b32_e32 v186, 1, v188
	v_lshl_add_u64 v[98:99], s[14:15], 0, v[186:187]
	s_lshl_b64 s[2:3], s[2:3], 8
	v_add_co_u32_e32 v98, vcc, s24, v98
	v_lshl_add_u64 v[114:115], v[190:191], 0, s[2:3]
	v_lshl_add_u64 v[116:117], v[192:193], 0, s[12:13]
	v_addc_co_u32_e32 v99, vcc, 0, v99, vcc
	global_load_dwordx4 v[146:149], v186, s[14:15]
	global_load_dwordx4 v[142:145], v186, s[14:15] offset:1024
	global_load_dwordx4 v[126:129], v186, s[14:15] offset:2048
	global_load_dwordx4 v[130:133], v186, s[14:15] offset:3072
	global_load_dwordx4 v[158:161], v[114:115], off
	global_load_dwordx4 v[138:141], v[114:115], off offset:64
	global_load_dwordx4 v[118:121], v220, s[14:15]
	global_load_dwordx4 v[122:125], v[98:99], off offset:1024
	global_load_dwordx4 v[110:113], v221, s[14:15]
	s_nop 0
	global_load_dwordx4 v[98:101], v[98:99], off offset:3072
	s_nop 0
	global_load_dwordx2 v[216:217], v[116:117], off
	global_load_dwordx2 v[212:213], v[116:117], off offset:512
	global_load_dwordx2 v[208:209], v[116:117], off offset:1024
	global_load_dwordx2 v[206:207], v[116:117], off offset:1536
	global_load_dwordx4 v[134:137], v[114:115], off offset:128
	s_nop 0
	global_load_dwordx4 v[114:117], v[114:115], off offset:192
	s_cmp_gt_u32 s20, 7
	s_cselect_b64 s[12:13], -1, 0
	s_cmp_lt_u32 s20, 8
	s_cbranch_scc1 .LBB0_3623
	s_add_i32 s14, s9, 0
	s_add_i32 s14, s14, 0x10020
	s_waitcnt lgkmcnt(0)
	v_add_u32_e32 v162, 8, v230
	v_cmp_lt_u32_e32 vcc, s20, v162
	s_cbranch_vccnz .LBB0_3623

.LBB0_3623:
	s_lshl_b32 s2, s20, 11
	s_and_b32 s2, s2, 0x3000
	v_add_u32_e32 v162, s2, v189
	v_cvt_pk_bf16_f32 v174, v154, v155
	v_cvt_pk_bf16_f32 v175, v156, v157
	v_cvt_pk_bf16_f32 v176, v150, v151
	v_cvt_pk_bf16_f32 v177, v152, v153
	v_cvt_pk_bf16_f32 v178, v102, v103
	v_cvt_pk_bf16_f32 v179, v104, v105
	v_cvt_pk_bf16_f32 v180, v106, v107
	v_cvt_pk_bf16_f32 v181, v108, v109
	ds_write2st64_b64 v162, v[174:175], v[176:177] offset1:1
	ds_write2st64_b64 v162, v[178:179], v[180:181] offset0:2 offset1:3
	s_nop 1
	s_or_b32 s17, s20, 1
	v_mov_b32_e32 v222, s9
	v_add_u32_e32 v222, 0x10000, v222
	v_add_u32_e32 v231, 32, v222
	v_mov_b32_e32 v223, s17
	s_waitcnt vmcnt(37)
	v_lshlrev_b32_e32 v162, 16, v196
	v_and_b32_e32 v163, 0xffff0000, v196
	v_pk_fma_f32 v[46:47], v[154:155], v[46:47], v[162:163]
	v_lshlrev_b32_e32 v154, 16, v197
	v_and_b32_e32 v155, 0xffff0000, v197
	v_pk_fma_f32 v[48:49], v[156:157], v[48:49], v[154:155]
	s_sub_i32 s15, 0x7c, s20
	s_add_i32 s14, s20, 3
	v_mfma_f32_16x16x32_bf16 v[42:45], v[42:45], v[174:177], v[46:49]
	s_and_b64 s[2:3], s[6:7], exec
	s_cselect_b32 s2, s14, s15
	s_add_i32 s2, s2, s21
	v_mfma_f32_16x16x32_bf16 v[170:173], v[34:37], v[178:181], v[42:45]
	s_waitcnt lgkmcnt(0)
	s_mov_b64 s[98:99], exec
	s_mov_b64 exec, s[0:1]
	ds_write_b32 v222, v223
	s_mov_b64 exec, s[98:99]
	ds_read_b32 v230, v231
	s_waitcnt vmcnt(36)
	v_lshlrev_b32_e32 v34, 16, v184
	v_and_b32_e32 v35, 0xffff0000, v184
	v_pk_fma_f32 v[26:27], v[150:151], v[26:27], v[34:35]
	v_lshlrev_b32_e32 v34, 16, v185
	v_and_b32_e32 v35, 0xffff0000, v185
	v_pk_fma_f32 v[28:29], v[152:153], v[28:29], v[34:35]
	s_ashr_i32 s3, s2, 31
	s_lshl_b64 s[26:27], s[2:3], 13
	v_mfma_f32_16x16x32_bf16 v[18:21], v[18:21], v[174:177], v[26:29]
	s_add_u32 s28, s22, s26
	s_addc_u32 s29, s23, s27
	s_lshl_b64 s[2:3], s[2:3], 8
	v_mfma_f32_16x16x32_bf16 v[166:169], v[22:25], v[178:181], v[18:21]
	v_lshl_add_u64 v[22:23], v[190:191], 0, s[2:3]
	v_lshl_add_u64 v[24:25], v[192:193], 0, s[26:27]
	global_load_dwordx4 v[154:157], v186, s[28:29]
	global_load_dwordx4 v[150:153], v186, s[28:29] offset:1024
	s_waitcnt vmcnt(37)
	v_lshlrev_b32_e32 v18, 16, v182
	v_and_b32_e32 v19, 0xffff0000, v182
	v_lshlrev_b32_e32 v20, 16, v183
	v_and_b32_e32 v21, 0xffff0000, v183
	s_waitcnt vmcnt(35)
	v_pk_fma_f32 v[18:19], v[102:103], v[30:31], v[18:19]
	v_pk_fma_f32 v[20:21], v[104:105], v[32:33], v[20:21]
	s_waitcnt vmcnt(29)
	s_nop 0
	v_mfma_f32_16x16x32_bf16 v[182:185], v[38:41], v[174:177], v[18:21]
	global_load_dwordx4 v[34:37], v186, s[28:29] offset:2048
	global_load_dwordx4 v[38:41], v186, s[28:29] offset:3072
	global_load_dwordx4 v[162:165], v[22:23], off
	global_load_dwordx4 v[46:49], v[22:23], off offset:64
	v_lshl_add_u64 v[18:19], s[28:29], 0, v[186:187]
	v_add_co_u32_e32 v42, vcc, 0x1000, v18
	v_mfma_f32_16x16x32_bf16 v[182:185], v[10:13], v[178:181], v[182:185]
	s_nop 0
	v_addc_co_u32_e32 v43, vcc, 0, v19, vcc
	global_load_dwordx4 v[26:29], v220, s[28:29]
	global_load_dwordx4 v[18:21], v221, s[28:29]
	global_load_dwordx4 v[30:33], v[42:43], off offset:1024
	global_load_dwordx4 v[102:105], v[42:43], off offset:3072
	global_load_dwordx2 v[218:219], v[24:25], off
	global_load_dwordx2 v[214:215], v[24:25], off offset:512
	global_load_dwordx2 v[210:211], v[24:25], off offset:1024
	global_load_dwordx2 v[196:197], v[24:25], off offset:1536
	s_nop 0
	global_load_dwordx4 v[42:45], v[22:23], off offset:128
	s_nop 0
	global_load_dwordx4 v[22:25], v[22:23], off offset:192
	v_lshlrev_b32_e32 v10, 16, v194
	v_and_b32_e32 v11, 0xffff0000, v194
	v_pk_fma_f32 v[6:7], v[106:107], v[6:7], v[10:11]
	v_lshlrev_b32_e32 v10, 16, v195
	v_and_b32_e32 v11, 0xffff0000, v195
	v_pk_fma_f32 v[8:9], v[108:109], v[8:9], v[10:11]
	s_andn2_b64 vcc, exec, s[12:13]
	s_waitcnt vmcnt(41)
	v_mfma_f32_16x16x32_bf16 v[6:9], v[14:17], v[174:177], v[6:9]
	v_mfma_f32_16x16x32_bf16 v[106:109], v[2:5], v[178:181], v[6:9]
	s_cbranch_vccnz .LBB0_3628
	s_add_i32 s12, s9, 0
	s_add_i32 s12, s12, 0x10020
	s_waitcnt lgkmcnt(0)
	v_add_u32_e32 v2, 8, v230
	v_cmp_lt_u32_e32 vcc, s17, v2
	s_cbranch_vccnz .LBB0_3628

.LBB0_3628:
	s_lshl_b32 s2, s17, 11
	s_and_b32 s2, s2, 0x3800
	v_add_u32_e32 v2, s2, v189
	v_cvt_pk_bf16_f32 v174, v170, v171
	v_cvt_pk_bf16_f32 v175, v172, v173
	v_cvt_pk_bf16_f32 v176, v166, v167
	v_cvt_pk_bf16_f32 v177, v168, v169
	v_cvt_pk_bf16_f32 v14, v182, v183
	v_cvt_pk_bf16_f32 v15, v184, v185
	v_cvt_pk_bf16_f32 v16, v106, v107
	v_cvt_pk_bf16_f32 v17, v108, v109
	ds_write2st64_b64 v2, v[174:175], v[176:177] offset1:1
	ds_write2st64_b64 v2, v[14:15], v[16:17] offset0:2 offset1:3
	s_nop 1
	v_mov_b32_e32 v222, s9
	v_add_u32_e32 v222, 0x10000, v222
	v_add_u32_e32 v231, 32, v222
	v_mov_b32_e32 v223, s16
	s_waitcnt vmcnt(37)
	v_lshlrev_b32_e32 v2, 16, v204
	v_and_b32_e32 v3, 0xffff0000, v204
	v_lshlrev_b32_e32 v4, 16, v205
	v_and_b32_e32 v5, 0xffff0000, v205
	v_pk_fma_f32 v[2:3], v[94:95], v[170:171], v[2:3]
	v_pk_fma_f32 v[4:5], v[96:97], v[172:173], v[4:5]
	s_sub_i32 s12, 0x7b, s20
	s_add_i32 s15, s20, 4
	v_mfma_f32_16x16x32_bf16 v[2:5], v[86:89], v[174:177], v[2:5]
	s_and_b64 s[2:3], s[6:7], exec
	s_cselect_b32 s2, s15, s12
	s_add_i32 s2, s2, s21
	s_waitcnt vmcnt(35)
	v_lshlrev_b32_e32 v6, 16, v200
	v_and_b32_e32 v7, 0xffff0000, v200
	v_lshlrev_b32_e32 v8, 16, v201
	v_and_b32_e32 v9, 0xffff0000, v201
	s_ashr_i32 s3, s2, 31
	v_mfma_f32_16x16x32_bf16 v[10:13], v[78:81], v[14:17], v[2:5]
	s_waitcnt lgkmcnt(0)
	s_mov_b64 s[98:99], exec
	s_mov_b64 exec, s[0:1]
	ds_write_b32 v222, v223
	s_mov_b64 exec, s[98:99]
	ds_read_b32 v230, v231
	s_waitcnt vmcnt(33)
	v_pk_fma_f32 v[6:7], v[90:91], v[182:183], v[6:7]
	v_pk_fma_f32 v[8:9], v[92:93], v[184:185], v[8:9]
	s_lshl_b64 s[12:13], s[2:3], 13
	v_lshlrev_b32_e32 v2, 16, v202
	v_and_b32_e32 v3, 0xffff0000, v202
	v_lshlrev_b32_e32 v4, 16, v203
	v_and_b32_e32 v5, 0xffff0000, v203
	v_pk_fma_f32 v[2:3], v[82:83], v[166:167], v[2:3]
	v_pk_fma_f32 v[4:5], v[84:85], v[168:169], v[4:5]
	v_mfma_f32_16x16x32_bf16 v[6:9], v[58:61], v[174:177], v[6:9]
	v_lshlrev_b32_e32 v58, 16, v198
	v_and_b32_e32 v59, 0xffff0000, v198
	v_lshlrev_b32_e32 v60, 16, v199
	v_and_b32_e32 v61, 0xffff0000, v199
	s_add_u32 s26, s22, s12
	v_mfma_f32_16x16x32_bf16 v[2:5], v[62:65], v[174:177], v[2:5]
	s_waitcnt vmcnt(32)
	v_pk_fma_f32 v[58:59], v[74:75], v[106:107], v[58:59]
	v_pk_fma_f32 v[60:61], v[76:77], v[108:109], v[60:61]
	s_addc_u32 s27, s23, s13
	s_lshl_b64 s[2:3], s[2:3], 8
	v_mfma_f32_16x16x32_bf16 v[166:169], v[54:57], v[174:177], v[58:61]
	v_lshl_add_u64 v[54:55], s[26:27], 0, v[186:187]
	v_add_co_u32_e32 v78, vcc, 0x1000, v54
	s_nop 0
	v_lshl_add_u64 v[58:59], v[190:191], 0, s[2:3]
	v_lshl_add_u64 v[60:61], v[192:193], 0, s[12:13]
	v_addc_co_u32_e32 v79, vcc, 0, v55, vcc
	v_mfma_f32_16x16x32_bf16 v[2:5], v[66:69], v[14:17], v[2:5]
	global_load_dwordx4 v[90:93], v186, s[26:27]
	global_load_dwordx4 v[86:89], v186, s[26:27] offset:1024
	s_cmp_lt_u32 s20, 6
	v_mfma_f32_16x16x32_bf16 v[6:9], v[70:73], v[14:17], v[6:9]
	global_load_dwordx4 v[70:73], v186, s[26:27] offset:2048
	global_load_dwordx4 v[74:77], v186, s[26:27] offset:3072
	global_load_dwordx4 v[94:97], v[58:59], off
	global_load_dwordx4 v[82:85], v[58:59], off offset:64
	global_load_dwordx4 v[62:65], v220, s[26:27]
	global_load_dwordx4 v[54:57], v221, s[26:27]
	global_load_dwordx4 v[66:69], v[78:79], off offset:1024
	global_load_dwordx4 v[106:109], v[78:79], off offset:3072
	global_load_dwordx2 v[202:203], v[60:61], off
	global_load_dwordx2 v[200:201], v[60:61], off offset:512
	global_load_dwordx2 v[198:199], v[60:61], off offset:1024
	global_load_dwordx2 v[178:179], v[60:61], off offset:1536
	s_nop 0
	global_load_dwordx4 v[78:81], v[58:59], off offset:128
	s_nop 0
	global_load_dwordx4 v[58:61], v[58:59], off offset:192
	v_mfma_f32_16x16x32_bf16 v[50:53], v[50:53], v[14:17], v[166:169]
	s_cbranch_scc1 .LBB0_3633
	s_add_i32 s12, s9, 0
	s_add_i32 s12, s12, 0x10020
	s_waitcnt lgkmcnt(0)
	v_add_u32_e32 v14, 8, v230
	v_cmp_lt_u32_e32 vcc, s16, v14
	s_cbranch_vccnz .LBB0_3633

.LBB0_3633:
	s_lshl_b32 s2, s16, 11
	s_and_b32 s2, s2, 0x3000
	v_add_u32_e32 v170, s2, v189
	v_cvt_pk_bf16_f32 v166, v10, v11
	v_cvt_pk_bf16_f32 v167, v12, v13
	v_cvt_pk_bf16_f32 v168, v2, v3
	v_cvt_pk_bf16_f32 v169, v4, v5
	v_cvt_pk_bf16_f32 v14, v6, v7
	v_cvt_pk_bf16_f32 v15, v8, v9
	v_cvt_pk_bf16_f32 v16, v50, v51
	v_cvt_pk_bf16_f32 v17, v52, v53
	ds_write2st64_b64 v170, v[166:167], v[168:169] offset1:1
	ds_write2st64_b64 v170, v[14:15], v[16:17] offset0:2 offset1:3
	s_nop 1
	v_mov_b32_e32 v222, s9
	v_add_u32_e32 v222, 0x10000, v222
	v_add_u32_e32 v231, 32, v222
	v_mov_b32_e32 v223, s14
	s_waitcnt vmcnt(37)
	v_lshlrev_b32_e32 v170, 16, v216
	v_and_b32_e32 v171, 0xffff0000, v216
	v_pk_fma_f32 v[10:11], v[158:159], v[10:11], v[170:171]
	v_lshlrev_b32_e32 v158, 16, v217
	v_and_b32_e32 v159, 0xffff0000, v217
	v_pk_fma_f32 v[12:13], v[160:161], v[12:13], v[158:159]
	s_sub_i32 s12, 0x7a, s20
	s_add_i32 s16, s20, 5
	v_mfma_f32_16x16x32_bf16 v[10:13], v[146:149], v[166:169], v[10:13]
	s_and_b64 s[2:3], s[6:7], exec
	s_cselect_b32 s2, s16, s12
	s_add_i32 s2, s2, s21
	v_mfma_f32_16x16x32_bf16 v[10:13], v[142:145], v[14:17], v[10:13]
	s_waitcnt lgkmcnt(0)
	s_mov_b64 s[98:99], exec
	s_mov_b64 exec, s[0:1]
	ds_write_b32 v222, v223
	s_mov_b64 exec, s[98:99]
	ds_read_b32 v230, v231
	s_waitcnt vmcnt(36)
	v_lshlrev_b32_e32 v142, 16, v212
	v_and_b32_e32 v143, 0xffff0000, v212
	v_pk_fma_f32 v[2:3], v[138:139], v[2:3], v[142:143]
	v_lshlrev_b32_e32 v138, 16, v213
	v_and_b32_e32 v139, 0xffff0000, v213
	v_pk_fma_f32 v[4:5], v[140:141], v[4:5], v[138:139]
	s_ashr_i32 s3, s2, 31
	s_lshl_b64 s[12:13], s[2:3], 13
	v_mfma_f32_16x16x32_bf16 v[2:5], v[126:129], v[166:169], v[2:5]
	s_waitcnt vmcnt(35)
	v_lshlrev_b32_e32 v126, 16, v208
	v_and_b32_e32 v127, 0xffff0000, v208
	s_waitcnt vmcnt(33)
	v_pk_fma_f32 v[6:7], v[134:135], v[6:7], v[126:127]
	v_lshlrev_b32_e32 v126, 16, v209
	v_and_b32_e32 v127, 0xffff0000, v209
	v_pk_fma_f32 v[8:9], v[136:137], v[8:9], v[126:127]
	s_add_u32 s26, s22, s12
	s_addc_u32 s27, s23, s13
	v_mfma_f32_16x16x32_bf16 v[6:9], v[118:121], v[166:169], v[6:9]
	v_lshlrev_b32_e32 v118, 16, v206
	v_and_b32_e32 v119, 0xffff0000, v206
	s_waitcnt vmcnt(32)
	v_pk_fma_f32 v[50:51], v[114:115], v[50:51], v[118:119]
	v_lshlrev_b32_e32 v114, 16, v207
	v_and_b32_e32 v115, 0xffff0000, v207
	v_pk_fma_f32 v[52:53], v[116:117], v[52:53], v[114:115]
	s_lshl_b64 s[2:3], s[2:3], 8
	v_lshl_add_u64 v[118:119], v[190:191], 0, s[2:3]
	v_mfma_f32_16x16x32_bf16 v[50:53], v[110:113], v[166:169], v[50:53]
	v_lshl_add_u64 v[110:111], s[26:27], 0, v[186:187]
	v_add_co_u32_e32 v110, vcc, 0x1000, v110
	v_lshl_add_u64 v[120:121], v[192:193], 0, s[12:13]
	s_nop 0
	v_addc_co_u32_e32 v111, vcc, 0, v111, vcc
	v_mfma_f32_16x16x32_bf16 v[2:5], v[130:133], v[14:17], v[2:5]
	global_load_dwordx4 v[158:161], v186, s[26:27]
	global_load_dwordx4 v[146:149], v186, s[26:27] offset:1024
	global_load_dwordx4 v[130:133], v186, s[26:27] offset:2048
	global_load_dwordx4 v[134:137], v186, s[26:27] offset:3072
	global_load_dwordx4 v[166:169], v[118:119], off
	global_load_dwordx4 v[142:145], v[118:119], off offset:64
	s_cmp_lt_u32 s20, 5
	v_mfma_f32_16x16x32_bf16 v[6:9], v[122:125], v[14:17], v[6:9]
	global_load_dwordx4 v[122:125], v220, s[26:27]
	global_load_dwordx4 v[114:117], v221, s[26:27]
	global_load_dwordx4 v[126:129], v[110:111], off offset:1024
	s_nop 0
	global_load_dwordx4 v[110:113], v[110:111], off offset:3072
	s_nop 0
	global_load_dwordx2 v[212:213], v[120:121], off
	global_load_dwordx2 v[208:209], v[120:121], off offset:512
	global_load_dwordx2 v[206:207], v[120:121], off offset:1024
	global_load_dwordx2 v[180:181], v[120:121], off offset:1536
	global_load_dwordx4 v[138:141], v[118:119], off offset:128
	s_nop 0
	global_load_dwordx4 v[118:121], v[118:119], off offset:192
	v_mfma_f32_16x16x32_bf16 v[14:17], v[98:101], v[14:17], v[50:53]
	s_cbranch_scc1 .LBB0_3638
	s_add_i32 s12, s9, 0
	s_add_i32 s12, s12, 0x10020
	s_waitcnt lgkmcnt(0)
	v_add_u32_e32 v50, 8, v230
	v_cmp_lt_u32_e32 vcc, s14, v50
	s_cbranch_vccnz .LBB0_3638

.LBB0_3638:
	s_lshl_b32 s2, s14, 11
	s_and_b32 s2, s2, 0x3800
	v_add_u32_e32 v50, s2, v189
	v_cvt_pk_bf16_f32 v174, v10, v11
	v_cvt_pk_bf16_f32 v175, v12, v13
	v_cvt_pk_bf16_f32 v176, v2, v3
	v_cvt_pk_bf16_f32 v177, v4, v5
	v_cvt_pk_bf16_f32 v170, v6, v7
	v_cvt_pk_bf16_f32 v171, v8, v9
	v_cvt_pk_bf16_f32 v172, v14, v15
	v_cvt_pk_bf16_f32 v173, v16, v17
	ds_write2st64_b64 v50, v[174:175], v[176:177] offset1:1
	ds_write2st64_b64 v50, v[170:171], v[172:173] offset0:2 offset1:3
	s_nop 1
	v_mov_b32_e32 v222, s9
	v_add_u32_e32 v222, 0x10000, v222
	v_add_u32_e32 v231, 32, v222
	v_mov_b32_e32 v223, s15
	s_waitcnt vmcnt(37)
	v_lshlrev_b32_e32 v50, 16, v218
	v_and_b32_e32 v51, 0xffff0000, v218
	v_pk_fma_f32 v[10:11], v[162:163], v[10:11], v[50:51]
	v_lshlrev_b32_e32 v50, 16, v219
	v_and_b32_e32 v51, 0xffff0000, v219
	v_pk_fma_f32 v[12:13], v[164:165], v[12:13], v[50:51]
	s_sub_i32 s12, 0x79, s20
	s_add_i32 s14, s20, 6
	v_mfma_f32_16x16x32_bf16 v[10:13], v[154:157], v[174:177], v[10:13]
	s_and_b64 s[2:3], s[6:7], exec
	s_cselect_b32 s2, s14, s12
	s_add_i32 s2, s2, s21
	v_mfma_f32_16x16x32_bf16 v[150:153], v[150:153], v[170:173], v[10:13]
	s_waitcnt lgkmcnt(0)
	s_mov_b64 s[98:99], exec
	s_mov_b64 exec, s[0:1]
	ds_write_b32 v222, v223
	s_mov_b64 exec, s[98:99]
	ds_read_b32 v230, v231
	s_ashr_i32 s3, s2, 31
	s_lshl_b64 s[12:13], s[2:3], 13
	s_add_u32 s26, s22, s12
	s_waitcnt vmcnt(36)
	v_lshlrev_b32_e32 v10, 16, v214
	v_and_b32_e32 v11, 0xffff0000, v214
	v_pk_fma_f32 v[2:3], v[46:47], v[2:3], v[10:11]
	v_lshlrev_b32_e32 v10, 16, v215
	v_and_b32_e32 v11, 0xffff0000, v215
	v_pk_fma_f32 v[4:5], v[48:49], v[4:5], v[10:11]
	s_addc_u32 s27, s23, s13
	s_lshl_b64 s[2:3], s[2:3], 8
	v_mfma_f32_16x16x32_bf16 v[2:5], v[34:37], v[174:177], v[2:5]
	s_cmp_lt_u32 s20, 4
	v_mfma_f32_16x16x32_bf16 v[50:53], v[38:41], v[170:173], v[2:5]
	s_waitcnt vmcnt(35)
	s_nop 4
	v_lshlrev_b32_e32 v2, 16, v210
	v_and_b32_e32 v3, 0xffff0000, v210
	v_lshlrev_b32_e32 v4, 16, v211
	v_and_b32_e32 v5, 0xffff0000, v211
	s_waitcnt vmcnt(33)
	v_pk_fma_f32 v[2:3], v[42:43], v[6:7], v[2:3]
	v_pk_fma_f32 v[4:5], v[44:45], v[8:9], v[4:5]
	v_lshl_add_u64 v[6:7], v[190:191], 0, s[2:3]
	v_lshl_add_u64 v[8:9], v[192:193], 0, s[12:13]
	v_mfma_f32_16x16x32_bf16 v[2:5], v[26:29], v[174:177], v[2:5]
	global_load_dwordx4 v[42:45], v186, s[26:27]
	global_load_dwordx4 v[34:37], v186, s[26:27] offset:1024
	v_mfma_f32_16x16x32_bf16 v[98:101], v[30:33], v[170:173], v[2:5]
	s_nop 4
	v_lshlrev_b32_e32 v2, 16, v196
	v_and_b32_e32 v3, 0xffff0000, v196
	v_lshlrev_b32_e32 v4, 16, v197
	v_and_b32_e32 v5, 0xffff0000, v197
	s_waitcnt vmcnt(34)
	v_pk_fma_f32 v[2:3], v[22:23], v[14:15], v[2:3]
	v_pk_fma_f32 v[4:5], v[24:25], v[16:17], v[4:5]
	s_nop 1
	v_mfma_f32_16x16x32_bf16 v[154:157], v[18:21], v[174:177], v[2:5]
	global_load_dwordx4 v[18:21], v186, s[26:27] offset:2048
	global_load_dwordx4 v[22:25], v186, s[26:27] offset:3072
	global_load_dwordx4 v[46:49], v[6:7], off
	global_load_dwordx4 v[26:29], v[6:7], off offset:64
	v_lshl_add_u64 v[2:3], s[26:27], 0, v[186:187]
	v_add_co_u32_e32 v2, vcc, 0x1000, v2
	v_mfma_f32_16x16x32_bf16 v[162:165], v[102:105], v[170:173], v[154:157]
	s_nop 0
	v_addc_co_u32_e32 v3, vcc, 0, v3, vcc
	global_load_dwordx4 v[38:41], v220, s[26:27]
	global_load_dwordx4 v[14:17], v221, s[26:27]
	global_load_dwordx4 v[10:13], v[2:3], off offset:1024
	s_nop 0
	global_load_dwordx4 v[2:5], v[2:3], off offset:3072
	s_nop 0
	global_load_dwordx2 v[196:197], v[8:9], off
	global_load_dwordx2 v[184:185], v[8:9], off offset:512
	global_load_dwordx2 v[182:183], v[8:9], off offset:1024
	global_load_dwordx2 v[194:195], v[8:9], off offset:1536
	global_load_dwordx4 v[30:33], v[6:7], off offset:128
	s_nop 0
	global_load_dwordx4 v[6:9], v[6:7], off offset:192
	s_cbranch_scc1 .LBB0_3643
	s_add_i32 s12, s9, 0
	s_add_i32 s12, s12, 0x10020
	s_waitcnt lgkmcnt(0)
	v_add_u32_e32 v102, 8, v230
	v_cmp_lt_u32_e32 vcc, s15, v102
	s_cbranch_vccnz .LBB0_3643

.LBB0_3643:
	s_lshl_b32 s2, s15, 11
	s_and_b32 s2, s2, 0x3000
	v_add_u32_e32 v102, s2, v189
	v_cvt_pk_bf16_f32 v170, v150, v151
	v_cvt_pk_bf16_f32 v171, v152, v153
	v_cvt_pk_bf16_f32 v172, v50, v51
	v_cvt_pk_bf16_f32 v173, v52, v53
	v_cvt_pk_bf16_f32 v154, v98, v99
	v_cvt_pk_bf16_f32 v155, v100, v101
	v_cvt_pk_bf16_f32 v156, v162, v163
	v_cvt_pk_bf16_f32 v157, v164, v165
	ds_write2st64_b64 v102, v[170:171], v[172:173] offset1:1
	ds_write2st64_b64 v102, v[154:155], v[156:157] offset0:2 offset1:3
	s_nop 1
	v_mov_b32_e32 v222, s9
	v_add_u32_e32 v222, 0x10000, v222
	v_add_u32_e32 v231, 32, v222
	v_mov_b32_e32 v223, s16
	s_waitcnt vmcnt(37)
	v_lshlrev_b32_e32 v102, 16, v202
	v_and_b32_e32 v103, 0xffff0000, v202
	v_pk_fma_f32 v[94:95], v[94:95], v[150:151], v[102:103]
	v_lshlrev_b32_e32 v102, 16, v203
	v_and_b32_e32 v103, 0xffff0000, v203
	v_pk_fma_f32 v[96:97], v[96:97], v[152:153], v[102:103]
	s_sub_i32 s12, 0x78, s20
	s_add_i32 s13, s20, 7
	v_mfma_f32_16x16x32_bf16 v[90:93], v[90:93], v[170:173], v[94:97]
	s_and_b64 s[2:3], s[6:7], exec
	s_cselect_b32 s2, s13, s12
	s_add_i32 s2, s2, s21
	v_mfma_f32_16x16x32_bf16 v[150:153], v[86:89], v[154:157], v[90:93]
	s_waitcnt lgkmcnt(0)
	s_mov_b64 s[98:99], exec
	s_mov_b64 exec, s[0:1]
	ds_write_b32 v222, v223
	s_mov_b64 exec, s[98:99]
	ds_read_b32 v230, v231
	s_waitcnt vmcnt(36)
	v_lshlrev_b32_e32 v86, 16, v200
	v_and_b32_e32 v87, 0xffff0000, v200
	v_pk_fma_f32 v[50:51], v[82:83], v[50:51], v[86:87]
	v_lshlrev_b32_e32 v82, 16, v201
	v_and_b32_e32 v83, 0xffff0000, v201
	v_pk_fma_f32 v[52:53], v[84:85], v[52:53], v[82:83]
	s_ashr_i32 s3, s2, 31
	s_lshl_b64 s[12:13], s[2:3], 13
	v_mfma_f32_16x16x32_bf16 v[50:53], v[70:73], v[170:173], v[50:53]
	s_add_u32 s26, s22, s12
	s_addc_u32 s27, s23, s13
	s_lshl_b64 s[2:3], s[2:3], 8
	v_mfma_f32_16x16x32_bf16 v[102:105], v[74:77], v[154:157], v[50:53]
	v_lshl_add_u64 v[74:75], v[190:191], 0, s[2:3]
	v_lshl_add_u64 v[76:77], v[192:193], 0, s[12:13]
	s_cmp_lt_u32 s20, 3
	s_waitcnt vmcnt(35)
	v_lshlrev_b32_e32 v50, 16, v198
	v_and_b32_e32 v51, 0xffff0000, v198
	v_lshlrev_b32_e32 v52, 16, v199
	v_and_b32_e32 v53, 0xffff0000, v199
	s_waitcnt vmcnt(33)
	v_pk_fma_f32 v[50:51], v[78:79], v[98:99], v[50:51]
	v_pk_fma_f32 v[52:53], v[80:81], v[100:101], v[52:53]
	global_load_dwordx4 v[86:89], v186, s[26:27]
	global_load_dwordx4 v[78:81], v186, s[26:27] offset:1024
	v_mfma_f32_16x16x32_bf16 v[50:53], v[62:65], v[170:173], v[50:53]
	v_mfma_f32_16x16x32_bf16 v[98:101], v[66:69], v[154:157], v[50:53]
	global_load_dwordx4 v[62:65], v186, s[26:27] offset:2048
	global_load_dwordx4 v[66:69], v186, s[26:27] offset:3072
	global_load_dwordx4 v[94:97], v[74:75], off
	global_load_dwordx4 v[82:85], v[74:75], off offset:64
	s_nop 2
	v_lshlrev_b32_e32 v50, 16, v178
	v_and_b32_e32 v51, 0xffff0000, v178
	v_lshlrev_b32_e32 v52, 16, v179
	v_and_b32_e32 v53, 0xffff0000, v179
	s_waitcnt vmcnt(38)
	v_pk_fma_f32 v[50:51], v[58:59], v[162:163], v[50:51]
	v_pk_fma_f32 v[52:53], v[60:61], v[164:165], v[52:53]
	s_nop 1
	v_mfma_f32_16x16x32_bf16 v[162:165], v[54:57], v[170:173], v[50:53]
	s_nop 2
	v_lshl_add_u64 v[50:51], s[26:27], 0, v[186:187]
	v_add_co_u32_e32 v50, vcc, 0x1000, v50
	v_mfma_f32_16x16x32_bf16 v[106:109], v[106:109], v[154:157], v[162:165]
	s_nop 0
	v_addc_co_u32_e32 v51, vcc, 0, v51, vcc
	global_load_dwordx4 v[58:61], v220, s[26:27]
	global_load_dwordx4 v[54:57], v221, s[26:27]
	global_load_dwordx4 v[70:73], v[50:51], off offset:1024
	s_nop 0
	global_load_dwordx4 v[50:53], v[50:51], off offset:3072
	s_nop 0
	global_load_dwordx2 v[204:205], v[76:77], off
	global_load_dwordx2 v[202:203], v[76:77], off offset:512
	global_load_dwordx2 v[200:201], v[76:77], off offset:1024
	global_load_dwordx2 v[198:199], v[76:77], off offset:1536
	global_load_dwordx4 v[90:93], v[74:75], off offset:128
	s_nop 0
	global_load_dwordx4 v[74:77], v[74:75], off offset:192
	s_cbranch_scc1 .LBB0_3648
	s_add_i32 s12, s9, 0
	s_add_i32 s12, s12, 0x10020
	s_waitcnt lgkmcnt(0)
	v_add_u32_e32 v154, 8, v230
	v_cmp_lt_u32_e32 vcc, s16, v154
	s_cbranch_vccnz .LBB0_3648

.LBB0_3648:
	s_lshl_b32 s2, s16, 11
	s_and_b32 s2, s2, 0x3800
	v_add_u32_e32 v154, s2, v189
	v_cvt_pk_bf16_f32 v170, v150, v151
	v_cvt_pk_bf16_f32 v171, v152, v153
	v_cvt_pk_bf16_f32 v172, v102, v103
	v_cvt_pk_bf16_f32 v173, v104, v105
	v_cvt_pk_bf16_f32 v162, v98, v99
	v_cvt_pk_bf16_f32 v163, v100, v101
	v_cvt_pk_bf16_f32 v164, v106, v107
	v_cvt_pk_bf16_f32 v165, v108, v109
	ds_write2st64_b64 v154, v[170:171], v[172:173] offset1:1
	ds_write2st64_b64 v154, v[162:163], v[164:165] offset0:2 offset1:3
	s_nop 1
	v_mov_b32_e32 v222, s9
	v_add_u32_e32 v222, 0x10000, v222
	v_add_u32_e32 v231, 32, v222
	v_mov_b32_e32 v223, s14
	s_waitcnt vmcnt(37)
	v_lshlrev_b32_e32 v154, 16, v212
	v_and_b32_e32 v155, 0xffff0000, v212
	v_pk_fma_f32 v[150:151], v[166:167], v[150:151], v[154:155]
	v_lshlrev_b32_e32 v154, 16, v213
	v_and_b32_e32 v155, 0xffff0000, v213
	v_pk_fma_f32 v[152:153], v[168:169], v[152:153], v[154:155]
	s_cmpk_lt_u32 s20, 0x78
	s_nop 0
	v_mfma_f32_16x16x32_bf16 v[150:153], v[158:161], v[170:173], v[150:153]
	v_mfma_f32_16x16x32_bf16 v[154:157], v[146:149], v[162:165], v[150:153]
	s_waitcnt lgkmcnt(0)
	s_mov_b64 s[98:99], exec
	s_mov_b64 exec, s[0:1]
	ds_write_b32 v222, v223
	s_mov_b64 exec, s[98:99]
	ds_read_b32 v230, v231
	s_waitcnt vmcnt(36)
	v_lshlrev_b32_e32 v146, 16, v208
	v_and_b32_e32 v147, 0xffff0000, v208
	v_pk_fma_f32 v[102:103], v[142:143], v[102:103], v[146:147]
	v_lshlrev_b32_e32 v142, 16, v209
	v_and_b32_e32 v143, 0xffff0000, v209
	v_pk_fma_f32 v[104:105], v[144:145], v[104:105], v[142:143]
	s_nop 1
	v_mfma_f32_16x16x32_bf16 v[102:105], v[130:133], v[170:173], v[102:105]
	v_mfma_f32_16x16x32_bf16 v[150:153], v[134:137], v[162:165], v[102:105]
	s_waitcnt vmcnt(35)
	s_nop 5
	v_lshlrev_b32_e32 v102, 16, v206
	v_and_b32_e32 v103, 0xffff0000, v206
	s_waitcnt vmcnt(33)
	v_pk_fma_f32 v[98:99], v[138:139], v[98:99], v[102:103]
	v_lshlrev_b32_e32 v102, 16, v207
	v_and_b32_e32 v103, 0xffff0000, v207
	v_pk_fma_f32 v[100:101], v[140:141], v[100:101], v[102:103]
	s_nop 1
	v_mfma_f32_16x16x32_bf16 v[98:101], v[122:125], v[170:173], v[98:101]
	v_mfma_f32_16x16x32_bf16 v[102:105], v[126:129], v[162:165], v[98:101]
	s_nop 6
	v_lshlrev_b32_e32 v98, 16, v180
	v_and_b32_e32 v99, 0xffff0000, v180
	v_lshlrev_b32_e32 v100, 16, v181
	v_and_b32_e32 v101, 0xffff0000, v181
	s_waitcnt vmcnt(32)
	v_pk_fma_f32 v[98:99], v[118:119], v[106:107], v[98:99]
	v_pk_fma_f32 v[100:101], v[120:121], v[108:109], v[100:101]
	s_nop 1
	v_mfma_f32_16x16x32_bf16 v[98:101], v[114:117], v[170:173], v[98:101]
	v_mfma_f32_16x16x32_bf16 v[106:109], v[110:113], v[162:165], v[98:101]
	s_cbranch_scc0 .LBB0_3652
	s_mov_b32 s20, s14
	s_branch .LBB0_3620
